# v21 + hand-written grid-barrier body: every workgroup watches the cross-XCD arrival counter directly (no release-generation relay, no integer divisions)
# baseline (speedup 1.0000x reference)
; __device__ __forceinline__ unsigned xb_ld(unsigned* p)              { return __hip_atomic_load(p, __ATOMIC_RELAXED, __HIP_MEMORY_SCOPE_AGENT); }
; __device__ __forceinline__ unsigned xb_add(unsigned* p, unsigned v) { return __hip_atomic_fetch_add(p, v, __ATOMIC_RELAXED, __HIP_MEMORY_SCOPE_AGENT); }
; #define XB_SPIN(cond, bar) do { unsigned _sp = 0; while (cond) { __builtin_amdgcn_s_sleep(1); \
;     if ((++_sp & 255u) == 0u) { if (xb_ld(&(bar)[XB_TMO])) break; if (_sp > XB_SPIN_CAP) { atomicAdd(&(bar)[XB_TMO], 1u); break; } } } } while (0)
; __device__ __forceinline__ void xcd_barrier(const XcdBarrier& b) {
;     asm volatile("s_waitcnt vmcnt(0)" ::: "memory");
;     __syncthreads();
;     if (threadIdx.x == 0) {
;         unsigned* bar = b.bar;
;         __builtin_amdgcn_s_waitcnt(0);
;         unsigned nloc = b.st[0], nx = b.st[1];
;         if (nloc == 0u) { xcd_barrier_complete(bar, b.x, nloc, nx); b.st[0] = nloc; b.st[1] = nx; }
;         const unsigned old = xb_add(&bar[XB_XSUB(b.x)], 1u);
;         const unsigned gen = old / nloc;
;         if (old + 1u == (gen + 1u) * nloc) {
;             __builtin_amdgcn_fence(__ATOMIC_RELEASE, "agent");
;             asm volatile("s_waitcnt vmcnt(0)" ::: "memory");
;             const unsigned og = xb_add(&bar[XB_TOP], 1u);
;             const unsigned tg = og / nx;
;             if (og + 1u == (tg + 1u) * nx) xb_add(&bar[XB_TOPGEN], 1u);
;             else XB_SPIN(xb_ld(&bar[XB_TOPGEN]) == tg, bar);
;             __builtin_amdgcn_fence(__ATOMIC_ACQUIRE, "agent");
;             xb_add(&bar[XB_XGEN(b.x)], 1u);
;             asm volatile("s_waitcnt vmcnt(0)" ::: "memory");
;         } else {
;             XB_SPIN(xb_ld(&bar[XB_XGEN(b.x)]) == gen, bar);
;             __builtin_amdgcn_fence(__ATOMIC_ACQUIRE, "agent");
;             asm volatile("s_waitcnt vmcnt(0)" ::: "memory");
;         }
.LBB0_228:
	s_waitcnt lgkmcnt(0)
	v_readfirstlane_b32 s8, v3
	v_readfirstlane_b32 s9, v1
	v_readlane_b32 s0, v252, 4
	s_lshl_b32 s0, s0, 8
	v_readlane_b32 s2, v252, 2
	v_readlane_b32 s3, v252, 3
	s_add_u32 s6, s2, s0
	s_addc_u32 s7, s3, 0
	s_mul_i32 s10, s8, 1
	s_mul_i32 s11, s9, 1
	v_mov_b32_e32 v4, 0x1000
	v_mov_b32_e32 v5, 1
	global_atomic_add v4, v4, v5, s[6:7] offset:1024 sc0
	v_mov_b32_e32 v1, 0x3400
	s_waitcnt vmcnt(0)
	v_readfirstlane_b32 s0, v4
	s_add_u32 s0, s0, 1
	s_cmp_lg_u32 s0, s10
	s_cbranch_scc1 .Lgbw_0
	buffer_wbl2 sc1
	s_waitcnt vmcnt(0)
	global_atomic_add v1, v5, s[2:3]
.Lgbw_0:
	s_mov_b32 s1, 0
.Lgbs_0:
	global_load_dword v2, v1, s[2:3] sc1
	s_waitcnt vmcnt(0)
	v_readfirstlane_b32 s0, v2
	s_cmp_ge_u32 s0, s11
	s_cbranch_scc1 .Lgbd_0
	s_sleep 1
	s_add_u32 s1, s1, 1
	s_cmp_lt_u32 s1, 0x40000
	s_cbranch_scc1 .Lgbs_0
.Lgbd_0:
	buffer_inv sc1
	s_waitcnt vmcnt(0)

; __device__ __forceinline__ unsigned xb_add(unsigned* p, unsigned v) { return __hip_atomic_fetch_add(p, v, __ATOMIC_RELAXED, __HIP_MEMORY_SCOPE_AGENT); }
; __device__ __forceinline__ void xcd_barrier(const XcdBarrier& b) {
;     ...
;     if (threadIdx.x == 0) {
;         unsigned* bar = b.bar;
;         __builtin_amdgcn_s_waitcnt(0);
;         unsigned nloc = b.st[0], nx = b.st[1];
;         if (nloc == 0u) { xcd_barrier_complete(bar, b.x, nloc, nx); b.st[0] = nloc; b.st[1] = nx; }
;         const unsigned old = xb_add(&bar[XB_XSUB(b.x)], 1u);
;         const unsigned gen = old / nloc;
;         if (old + 1u == (gen + 1u) * nloc) {
;             __builtin_amdgcn_fence(__ATOMIC_RELEASE, "agent");
;             asm volatile("s_waitcnt vmcnt(0)" ::: "memory");
;             const unsigned og = xb_add(&bar[XB_TOP], 1u);
;             const unsigned tg = og / nx;
;             if (og + 1u == (tg + 1u) * nx) xb_add(&bar[XB_TOPGEN], 1u);
.LBB0_312:
	s_waitcnt lgkmcnt(0)
	v_readfirstlane_b32 s8, v3
	v_readfirstlane_b32 s9, v1
	v_readlane_b32 s0, v252, 4
	s_lshl_b32 s0, s0, 8
	v_readlane_b32 s2, v252, 2
	v_readlane_b32 s3, v252, 3
	s_add_u32 s6, s2, s0
	s_addc_u32 s7, s3, 0
	s_mul_i32 s10, s8, 2
	s_mul_i32 s11, s9, 2
	v_mov_b32_e32 v4, 0x1000
	v_mov_b32_e32 v5, 1
	global_atomic_add v4, v4, v5, s[6:7] offset:1024 sc0
	v_mov_b32_e32 v1, 0x3400
	s_waitcnt vmcnt(0)
	v_readfirstlane_b32 s0, v4
	s_add_u32 s0, s0, 1
	s_cmp_lg_u32 s0, s10
	s_cbranch_scc1 .Lgbw_1
	buffer_wbl2 sc1
	s_waitcnt vmcnt(0)
	global_atomic_add v1, v5, s[2:3]

; __device__ __forceinline__ unsigned xb_add(unsigned* p, unsigned v) { return __hip_atomic_fetch_add(p, v, __ATOMIC_RELAXED, __HIP_MEMORY_SCOPE_AGENT); }
; __device__ __forceinline__ void xcd_barrier(const XcdBarrier& b) {
;     ...
;     if (threadIdx.x == 0) {
;         unsigned* bar = b.bar;
;         __builtin_amdgcn_s_waitcnt(0);
;         unsigned nloc = b.st[0], nx = b.st[1];
;         if (nloc == 0u) { xcd_barrier_complete(bar, b.x, nloc, nx); b.st[0] = nloc; b.st[1] = nx; }
;         const unsigned old = xb_add(&bar[XB_XSUB(b.x)], 1u);
;         const unsigned gen = old / nloc;
;         if (old + 1u == (gen + 1u) * nloc) {
;             __builtin_amdgcn_fence(__ATOMIC_RELEASE, "agent");
;             asm volatile("s_waitcnt vmcnt(0)" ::: "memory");
;             const unsigned og = xb_add(&bar[XB_TOP], 1u);
;             const unsigned tg = og / nx;
;             if (og + 1u == (tg + 1u) * nx) xb_add(&bar[XB_TOPGEN], 1u);
.LBB0_395:
	s_waitcnt lgkmcnt(0)
	v_readfirstlane_b32 s8, v3
	v_readfirstlane_b32 s9, v1
	v_readlane_b32 s0, v252, 4
	s_lshl_b32 s0, s0, 8
	v_readlane_b32 s2, v252, 2
	v_readlane_b32 s3, v252, 3
	s_add_u32 s6, s2, s0
	s_addc_u32 s7, s3, 0
	s_mul_i32 s10, s8, 3
	s_mul_i32 s11, s9, 3
	v_mov_b32_e32 v4, 0x1000
	v_mov_b32_e32 v5, 1
	global_atomic_add v4, v4, v5, s[6:7] offset:1024 sc0
	v_mov_b32_e32 v1, 0x3400
	s_waitcnt vmcnt(0)
	v_readfirstlane_b32 s0, v4
	s_add_u32 s0, s0, 1
	s_cmp_lg_u32 s0, s10
	s_cbranch_scc1 .Lgbw_2
	buffer_wbl2 sc1
	s_waitcnt vmcnt(0)
	global_atomic_add v1, v5, s[2:3]

; __device__ __forceinline__ unsigned xb_add(unsigned* p, unsigned v) { return __hip_atomic_fetch_add(p, v, __ATOMIC_RELAXED, __HIP_MEMORY_SCOPE_AGENT); }
; __device__ __forceinline__ void xcd_barrier(const XcdBarrier& b) {
;     ...
;     if (threadIdx.x == 0) {
;         unsigned* bar = b.bar;
;         __builtin_amdgcn_s_waitcnt(0);
;         unsigned nloc = b.st[0], nx = b.st[1];
;         if (nloc == 0u) { xcd_barrier_complete(bar, b.x, nloc, nx); b.st[0] = nloc; b.st[1] = nx; }
;         const unsigned old = xb_add(&bar[XB_XSUB(b.x)], 1u);
;         const unsigned gen = old / nloc;
;         if (old + 1u == (gen + 1u) * nloc) {
;             __builtin_amdgcn_fence(__ATOMIC_RELEASE, "agent");
;             asm volatile("s_waitcnt vmcnt(0)" ::: "memory");
;             const unsigned og = xb_add(&bar[XB_TOP], 1u);
;             const unsigned tg = og / nx;
;             if (og + 1u == (tg + 1u) * nx) xb_add(&bar[XB_TOPGEN], 1u);
.LBB0_489:
	s_waitcnt lgkmcnt(0)
	v_readfirstlane_b32 s8, v3
	v_readfirstlane_b32 s9, v1
	v_readlane_b32 s0, v252, 4
	s_lshl_b32 s0, s0, 8
	v_readlane_b32 s2, v252, 2
	v_readlane_b32 s3, v252, 3
	s_add_u32 s6, s2, s0
	s_addc_u32 s7, s3, 0
	s_mul_i32 s10, s8, 4
	s_mul_i32 s11, s9, 4
	v_mov_b32_e32 v4, 0x1000
	v_mov_b32_e32 v5, 1
	global_atomic_add v4, v4, v5, s[6:7] offset:1024 sc0
	v_mov_b32_e32 v1, 0x3400
	s_waitcnt vmcnt(0)
	v_readfirstlane_b32 s0, v4
	s_add_u32 s0, s0, 1
	s_cmp_lg_u32 s0, s10
	s_cbranch_scc1 .Lgbw_3
	buffer_wbl2 sc1
	s_waitcnt vmcnt(0)
	global_atomic_add v1, v5, s[2:3]

; __device__ __forceinline__ unsigned xb_add(unsigned* p, unsigned v) { return __hip_atomic_fetch_add(p, v, __ATOMIC_RELAXED, __HIP_MEMORY_SCOPE_AGENT); }
; __device__ __forceinline__ void xcd_barrier(const XcdBarrier& b) {
;     ...
;     if (threadIdx.x == 0) {
;         unsigned* bar = b.bar;
;         __builtin_amdgcn_s_waitcnt(0);
;         unsigned nloc = b.st[0], nx = b.st[1];
;         if (nloc == 0u) { xcd_barrier_complete(bar, b.x, nloc, nx); b.st[0] = nloc; b.st[1] = nx; }
;         const unsigned old = xb_add(&bar[XB_XSUB(b.x)], 1u);
;         const unsigned gen = old / nloc;
;         if (old + 1u == (gen + 1u) * nloc) {
;             __builtin_amdgcn_fence(__ATOMIC_RELEASE, "agent");
;             asm volatile("s_waitcnt vmcnt(0)" ::: "memory");
;             const unsigned og = xb_add(&bar[XB_TOP], 1u);
;             const unsigned tg = og / nx;
;             if (og + 1u == (tg + 1u) * nx) xb_add(&bar[XB_TOPGEN], 1u);
.LBB0_605:
	s_waitcnt lgkmcnt(0)
	v_readfirstlane_b32 s8, v3
	v_readfirstlane_b32 s9, v1
	v_readlane_b32 s0, v252, 4
	s_lshl_b32 s0, s0, 8
	v_readlane_b32 s2, v252, 2
	v_readlane_b32 s3, v252, 3
	s_add_u32 s6, s2, s0
	s_addc_u32 s7, s3, 0
	s_mul_i32 s10, s8, 5
	s_mul_i32 s11, s9, 5
	v_mov_b32_e32 v4, 0x1000
	v_mov_b32_e32 v5, 1
	global_atomic_add v4, v4, v5, s[6:7] offset:1024 sc0
	v_mov_b32_e32 v1, 0x3400
	s_waitcnt vmcnt(0)
	v_readfirstlane_b32 s0, v4
	s_add_u32 s0, s0, 1
	s_cmp_lg_u32 s0, s10
	s_cbranch_scc1 .Lgbw_4
	buffer_wbl2 sc1
	s_waitcnt vmcnt(0)
	global_atomic_add v1, v5, s[2:3]

; __device__ __forceinline__ unsigned xb_add(unsigned* p, unsigned v) { return __hip_atomic_fetch_add(p, v, __ATOMIC_RELAXED, __HIP_MEMORY_SCOPE_AGENT); }
; __device__ __forceinline__ void xcd_barrier(const XcdBarrier& b) {
;     ...
;     if (threadIdx.x == 0) {
;         unsigned* bar = b.bar;
;         __builtin_amdgcn_s_waitcnt(0);
;         unsigned nloc = b.st[0], nx = b.st[1];
;         if (nloc == 0u) { xcd_barrier_complete(bar, b.x, nloc, nx); b.st[0] = nloc; b.st[1] = nx; }
;         const unsigned old = xb_add(&bar[XB_XSUB(b.x)], 1u);
;         const unsigned gen = old / nloc;
;         if (old + 1u == (gen + 1u) * nloc) {
;             __builtin_amdgcn_fence(__ATOMIC_RELEASE, "agent");
;             asm volatile("s_waitcnt vmcnt(0)" ::: "memory");
;             const unsigned og = xb_add(&bar[XB_TOP], 1u);
;             const unsigned tg = og / nx;
;             if (og + 1u == (tg + 1u) * nx) xb_add(&bar[XB_TOPGEN], 1u);
.LBB0_691:
	s_waitcnt lgkmcnt(0)
	v_readfirstlane_b32 s8, v3
	v_readfirstlane_b32 s9, v1
	v_readlane_b32 s0, v252, 4
	s_lshl_b32 s0, s0, 8
	v_readlane_b32 s2, v252, 2
	v_readlane_b32 s3, v252, 3
	s_add_u32 s6, s2, s0
	s_addc_u32 s7, s3, 0
	s_mul_i32 s10, s8, 6
	s_mul_i32 s11, s9, 6
	v_mov_b32_e32 v4, 0x1000
	v_mov_b32_e32 v5, 1
	global_atomic_add v4, v4, v5, s[6:7] offset:1024 sc0
	v_mov_b32_e32 v1, 0x3400
	s_waitcnt vmcnt(0)
	v_readfirstlane_b32 s0, v4
	s_add_u32 s0, s0, 1
	s_cmp_lg_u32 s0, s10
	s_cbranch_scc1 .Lgbw_5
	buffer_wbl2 sc1
	s_waitcnt vmcnt(0)
	global_atomic_add v1, v5, s[2:3]

; __device__ __forceinline__ unsigned xb_add(unsigned* p, unsigned v) { return __hip_atomic_fetch_add(p, v, __ATOMIC_RELAXED, __HIP_MEMORY_SCOPE_AGENT); }
; __device__ __forceinline__ void xcd_barrier(const XcdBarrier& b) {
;     ...
;     if (threadIdx.x == 0) {
;         unsigned* bar = b.bar;
;         __builtin_amdgcn_s_waitcnt(0);
;         unsigned nloc = b.st[0], nx = b.st[1];
;         if (nloc == 0u) { xcd_barrier_complete(bar, b.x, nloc, nx); b.st[0] = nloc; b.st[1] = nx; }
;         const unsigned old = xb_add(&bar[XB_XSUB(b.x)], 1u);
;         const unsigned gen = old / nloc;
;         if (old + 1u == (gen + 1u) * nloc) {
;             __builtin_amdgcn_fence(__ATOMIC_RELEASE, "agent");
;             asm volatile("s_waitcnt vmcnt(0)" ::: "memory");
;             const unsigned og = xb_add(&bar[XB_TOP], 1u);
;             const unsigned tg = og / nx;
;             if (og + 1u == (tg + 1u) * nx) xb_add(&bar[XB_TOPGEN], 1u);
.LBB0_759:
	s_waitcnt lgkmcnt(0)
	v_readfirstlane_b32 s8, v3
	v_readfirstlane_b32 s9, v1
	v_readlane_b32 s0, v252, 4
	s_lshl_b32 s0, s0, 8
	v_readlane_b32 s2, v252, 2
	v_readlane_b32 s3, v252, 3
	s_add_u32 s6, s2, s0
	s_addc_u32 s7, s3, 0
	s_mul_i32 s10, s8, 7
	s_mul_i32 s11, s9, 7
	v_mov_b32_e32 v4, 0x1000
	v_mov_b32_e32 v5, 1
	global_atomic_add v4, v4, v5, s[6:7] offset:1024 sc0
	v_mov_b32_e32 v1, 0x3400
	s_waitcnt vmcnt(0)
	v_readfirstlane_b32 s0, v4
	s_add_u32 s0, s0, 1
	s_cmp_lg_u32 s0, s10
	s_cbranch_scc1 .Lgbw_6
	buffer_wbl2 sc1
	s_waitcnt vmcnt(0)
	global_atomic_add v1, v5, s[2:3]

; __device__ __forceinline__ unsigned xb_add(unsigned* p, unsigned v) { return __hip_atomic_fetch_add(p, v, __ATOMIC_RELAXED, __HIP_MEMORY_SCOPE_AGENT); }
; __device__ __forceinline__ void xcd_barrier(const XcdBarrier& b) {
;     ...
;     if (threadIdx.x == 0) {
;         unsigned* bar = b.bar;
;         __builtin_amdgcn_s_waitcnt(0);
;         unsigned nloc = b.st[0], nx = b.st[1];
;         if (nloc == 0u) { xcd_barrier_complete(bar, b.x, nloc, nx); b.st[0] = nloc; b.st[1] = nx; }
;         const unsigned old = xb_add(&bar[XB_XSUB(b.x)], 1u);
;         const unsigned gen = old / nloc;
;         if (old + 1u == (gen + 1u) * nloc) {
;             __builtin_amdgcn_fence(__ATOMIC_RELEASE, "agent");
;             asm volatile("s_waitcnt vmcnt(0)" ::: "memory");
;             const unsigned og = xb_add(&bar[XB_TOP], 1u);
;             const unsigned tg = og / nx;
;             if (og + 1u == (tg + 1u) * nx) xb_add(&bar[XB_TOPGEN], 1u);
.LBB0_827:
	s_waitcnt lgkmcnt(0)
	v_readfirstlane_b32 s8, v3
	v_readfirstlane_b32 s9, v1
	v_readlane_b32 s0, v252, 4
	s_lshl_b32 s0, s0, 8
	v_readlane_b32 s2, v252, 2
	v_readlane_b32 s3, v252, 3
	s_add_u32 s6, s2, s0
	s_addc_u32 s7, s3, 0
	s_mul_i32 s10, s8, 8
	s_mul_i32 s11, s9, 8
	v_mov_b32_e32 v4, 0x1000
	v_mov_b32_e32 v5, 1
	global_atomic_add v4, v4, v5, s[6:7] offset:1024 sc0
	v_mov_b32_e32 v1, 0x3400
	s_waitcnt vmcnt(0)
	v_readfirstlane_b32 s0, v4
	s_add_u32 s0, s0, 1
	s_cmp_lg_u32 s0, s10
	s_cbranch_scc1 .Lgbw_7
	buffer_wbl2 sc1
	s_waitcnt vmcnt(0)
	global_atomic_add v1, v5, s[2:3]

; __device__ __forceinline__ unsigned xb_add(unsigned* p, unsigned v) { return __hip_atomic_fetch_add(p, v, __ATOMIC_RELAXED, __HIP_MEMORY_SCOPE_AGENT); }
; __device__ __forceinline__ void xcd_barrier(const XcdBarrier& b) {
;     ...
;     if (threadIdx.x == 0) {
;         unsigned* bar = b.bar;
;         __builtin_amdgcn_s_waitcnt(0);
;         unsigned nloc = b.st[0], nx = b.st[1];
;         if (nloc == 0u) { xcd_barrier_complete(bar, b.x, nloc, nx); b.st[0] = nloc; b.st[1] = nx; }
;         const unsigned old = xb_add(&bar[XB_XSUB(b.x)], 1u);
;         const unsigned gen = old / nloc;
;         if (old + 1u == (gen + 1u) * nloc) {
;             __builtin_amdgcn_fence(__ATOMIC_RELEASE, "agent");
;             asm volatile("s_waitcnt vmcnt(0)" ::: "memory");
;             const unsigned og = xb_add(&bar[XB_TOP], 1u);
;             const unsigned tg = og / nx;
;             if (og + 1u == (tg + 1u) * nx) xb_add(&bar[XB_TOPGEN], 1u);
.LBB0_961:
	s_waitcnt lgkmcnt(0)
	v_readfirstlane_b32 s8, v3
	v_readfirstlane_b32 s9, v1
	v_readlane_b32 s0, v252, 4
	s_lshl_b32 s0, s0, 8
	v_readlane_b32 s2, v252, 2
	v_readlane_b32 s3, v252, 3
	s_add_u32 s6, s2, s0
	s_addc_u32 s7, s3, 0
	s_mul_i32 s10, s8, 9
	s_mul_i32 s11, s9, 9
	v_mov_b32_e32 v4, 0x1000
	v_mov_b32_e32 v5, 1
	global_atomic_add v4, v4, v5, s[6:7] offset:1024 sc0
	v_mov_b32_e32 v1, 0x3400
	s_waitcnt vmcnt(0)
	v_readfirstlane_b32 s0, v4
	s_add_u32 s0, s0, 1
	s_cmp_lg_u32 s0, s10
	s_cbranch_scc1 .Lgbw_8
	buffer_wbl2 sc1
	s_waitcnt vmcnt(0)
	global_atomic_add v1, v5, s[2:3]

; __device__ __forceinline__ unsigned xb_add(unsigned* p, unsigned v) { return __hip_atomic_fetch_add(p, v, __ATOMIC_RELAXED, __HIP_MEMORY_SCOPE_AGENT); }
; __device__ __forceinline__ void xcd_barrier(const XcdBarrier& b) {
;     ...
;     if (threadIdx.x == 0) {
;         unsigned* bar = b.bar;
;         __builtin_amdgcn_s_waitcnt(0);
;         unsigned nloc = b.st[0], nx = b.st[1];
;         if (nloc == 0u) { xcd_barrier_complete(bar, b.x, nloc, nx); b.st[0] = nloc; b.st[1] = nx; }
;         const unsigned old = xb_add(&bar[XB_XSUB(b.x)], 1u);
;         const unsigned gen = old / nloc;
;         if (old + 1u == (gen + 1u) * nloc) {
;             __builtin_amdgcn_fence(__ATOMIC_RELEASE, "agent");
;             asm volatile("s_waitcnt vmcnt(0)" ::: "memory");
;             const unsigned og = xb_add(&bar[XB_TOP], 1u);
;             const unsigned tg = og / nx;
;             if (og + 1u == (tg + 1u) * nx) xb_add(&bar[XB_TOPGEN], 1u);
.LBB0_1105:
	s_waitcnt lgkmcnt(0)
	v_readfirstlane_b32 s8, v3
	v_readfirstlane_b32 s9, v1
	v_readlane_b32 s0, v252, 4
	s_lshl_b32 s0, s0, 8
	v_readlane_b32 s2, v252, 2
	v_readlane_b32 s3, v252, 3
	s_add_u32 s6, s2, s0
	s_addc_u32 s7, s3, 0
	s_mul_i32 s10, s8, 10
	s_mul_i32 s11, s9, 10
	v_mov_b32_e32 v4, 0x1000
	v_mov_b32_e32 v5, 1
	global_atomic_add v4, v4, v5, s[6:7] offset:1024 sc0
	v_mov_b32_e32 v1, 0x3400
	s_waitcnt vmcnt(0)
	v_readfirstlane_b32 s0, v4
	s_add_u32 s0, s0, 1
	s_cmp_lg_u32 s0, s10
	s_cbranch_scc1 .Lgbw_9
	buffer_wbl2 sc1
	s_waitcnt vmcnt(0)
	global_atomic_add v1, v5, s[2:3]

; __device__ __forceinline__ unsigned xb_add(unsigned* p, unsigned v) { return __hip_atomic_fetch_add(p, v, __ATOMIC_RELAXED, __HIP_MEMORY_SCOPE_AGENT); }
; __device__ __forceinline__ void xcd_barrier(const XcdBarrier& b) {
;     ...
;     if (threadIdx.x == 0) {
;         unsigned* bar = b.bar;
;         __builtin_amdgcn_s_waitcnt(0);
;         unsigned nloc = b.st[0], nx = b.st[1];
;         if (nloc == 0u) { xcd_barrier_complete(bar, b.x, nloc, nx); b.st[0] = nloc; b.st[1] = nx; }
;         const unsigned old = xb_add(&bar[XB_XSUB(b.x)], 1u);
;         const unsigned gen = old / nloc;
;         if (old + 1u == (gen + 1u) * nloc) {
;             __builtin_amdgcn_fence(__ATOMIC_RELEASE, "agent");
;             asm volatile("s_waitcnt vmcnt(0)" ::: "memory");
;             const unsigned og = xb_add(&bar[XB_TOP], 1u);
;             const unsigned tg = og / nx;
;             if (og + 1u == (tg + 1u) * nx) xb_add(&bar[XB_TOPGEN], 1u);
.LBB0_1192:
	s_waitcnt lgkmcnt(0)
	v_readfirstlane_b32 s8, v3
	v_readfirstlane_b32 s9, v1
	v_readlane_b32 s0, v252, 4
	s_lshl_b32 s0, s0, 8
	v_readlane_b32 s2, v252, 2
	v_readlane_b32 s3, v252, 3
	s_add_u32 s6, s2, s0
	s_addc_u32 s7, s3, 0
	s_mul_i32 s10, s8, 11
	s_mul_i32 s11, s9, 11
	v_mov_b32_e32 v4, 0x1000
	v_mov_b32_e32 v5, 1
	global_atomic_add v4, v4, v5, s[6:7] offset:1024 sc0
	v_mov_b32_e32 v1, 0x3400
	s_waitcnt vmcnt(0)
	v_readfirstlane_b32 s0, v4
	s_add_u32 s0, s0, 1
	s_cmp_lg_u32 s0, s10
	s_cbranch_scc1 .Lgbw_10
	buffer_wbl2 sc1
	s_waitcnt vmcnt(0)
	global_atomic_add v1, v5, s[2:3]

; __device__ __forceinline__ unsigned xb_add(unsigned* p, unsigned v) { return __hip_atomic_fetch_add(p, v, __ATOMIC_RELAXED, __HIP_MEMORY_SCOPE_AGENT); }
; __device__ __forceinline__ void xcd_barrier(const XcdBarrier& b) {
;     ...
;     if (threadIdx.x == 0) {
;         unsigned* bar = b.bar;
;         __builtin_amdgcn_s_waitcnt(0);
;         unsigned nloc = b.st[0], nx = b.st[1];
;         if (nloc == 0u) { xcd_barrier_complete(bar, b.x, nloc, nx); b.st[0] = nloc; b.st[1] = nx; }
;         const unsigned old = xb_add(&bar[XB_XSUB(b.x)], 1u);
;         const unsigned gen = old / nloc;
;         if (old + 1u == (gen + 1u) * nloc) {
;             __builtin_amdgcn_fence(__ATOMIC_RELEASE, "agent");
;             asm volatile("s_waitcnt vmcnt(0)" ::: "memory");
;             const unsigned og = xb_add(&bar[XB_TOP], 1u);
;             const unsigned tg = og / nx;
;             if (og + 1u == (tg + 1u) * nx) xb_add(&bar[XB_TOPGEN], 1u);
.LBB0_1314:
	s_waitcnt lgkmcnt(0)
	v_readfirstlane_b32 s8, v3
	v_readfirstlane_b32 s9, v1
	v_readlane_b32 s0, v252, 4
	s_lshl_b32 s0, s0, 8
	v_readlane_b32 s2, v252, 2
	v_readlane_b32 s3, v252, 3
	s_add_u32 s6, s2, s0
	s_addc_u32 s7, s3, 0
	s_mul_i32 s10, s8, 12
	s_mul_i32 s11, s9, 12
	v_mov_b32_e32 v4, 0x1000
	v_mov_b32_e32 v5, 1
	global_atomic_add v4, v4, v5, s[6:7] offset:1024 sc0
	v_mov_b32_e32 v1, 0x3400
	s_waitcnt vmcnt(0)
	v_readfirstlane_b32 s0, v4
	s_add_u32 s0, s0, 1
	s_cmp_lg_u32 s0, s10
	s_cbranch_scc1 .Lgbw_11
	buffer_wbl2 sc1
	s_waitcnt vmcnt(0)
	global_atomic_add v1, v5, s[2:3]

; __device__ __forceinline__ unsigned xb_add(unsigned* p, unsigned v) { return __hip_atomic_fetch_add(p, v, __ATOMIC_RELAXED, __HIP_MEMORY_SCOPE_AGENT); }
; __device__ __forceinline__ void xcd_barrier(const XcdBarrier& b) {
;     ...
;     if (threadIdx.x == 0) {
;         unsigned* bar = b.bar;
;         __builtin_amdgcn_s_waitcnt(0);
;         unsigned nloc = b.st[0], nx = b.st[1];
;         if (nloc == 0u) { xcd_barrier_complete(bar, b.x, nloc, nx); b.st[0] = nloc; b.st[1] = nx; }
;         const unsigned old = xb_add(&bar[XB_XSUB(b.x)], 1u);
;         const unsigned gen = old / nloc;
;         if (old + 1u == (gen + 1u) * nloc) {
;             __builtin_amdgcn_fence(__ATOMIC_RELEASE, "agent");
;             asm volatile("s_waitcnt vmcnt(0)" ::: "memory");
;             const unsigned og = xb_add(&bar[XB_TOP], 1u);
;             const unsigned tg = og / nx;
;             if (og + 1u == (tg + 1u) * nx) xb_add(&bar[XB_TOPGEN], 1u);
.LBB0_1381:
	s_waitcnt lgkmcnt(0)
	v_readfirstlane_b32 s8, v3
	v_readfirstlane_b32 s9, v1
	v_readlane_b32 s0, v252, 4
	s_lshl_b32 s0, s0, 8
	v_readlane_b32 s2, v252, 2
	v_readlane_b32 s3, v252, 3
	s_add_u32 s6, s2, s0
	s_addc_u32 s7, s3, 0
	s_mul_i32 s10, s8, 13
	s_mul_i32 s11, s9, 13
	v_mov_b32_e32 v4, 0x1000
	v_mov_b32_e32 v5, 1
	global_atomic_add v4, v4, v5, s[6:7] offset:1024 sc0
	v_mov_b32_e32 v1, 0x3400
	s_waitcnt vmcnt(0)
	v_readfirstlane_b32 s0, v4
	s_add_u32 s0, s0, 1
	s_cmp_lg_u32 s0, s10
	s_cbranch_scc1 .Lgbw_12
	buffer_wbl2 sc1
	s_waitcnt vmcnt(0)
	global_atomic_add v1, v5, s[2:3]

; __device__ __forceinline__ unsigned xb_add(unsigned* p, unsigned v) { return __hip_atomic_fetch_add(p, v, __ATOMIC_RELAXED, __HIP_MEMORY_SCOPE_AGENT); }
; __device__ __forceinline__ void xcd_barrier(const XcdBarrier& b) {
;     ...
;     if (threadIdx.x == 0) {
;         unsigned* bar = b.bar;
;         __builtin_amdgcn_s_waitcnt(0);
;         unsigned nloc = b.st[0], nx = b.st[1];
;         if (nloc == 0u) { xcd_barrier_complete(bar, b.x, nloc, nx); b.st[0] = nloc; b.st[1] = nx; }
;         const unsigned old = xb_add(&bar[XB_XSUB(b.x)], 1u);
;         const unsigned gen = old / nloc;
;         if (old + 1u == (gen + 1u) * nloc) {
;             __builtin_amdgcn_fence(__ATOMIC_RELEASE, "agent");
;             asm volatile("s_waitcnt vmcnt(0)" ::: "memory");
;             const unsigned og = xb_add(&bar[XB_TOP], 1u);
;             const unsigned tg = og / nx;
;             if (og + 1u == (tg + 1u) * nx) xb_add(&bar[XB_TOPGEN], 1u);
.LBB0_1499:
	s_waitcnt lgkmcnt(0)
	v_readfirstlane_b32 s8, v3
	v_readfirstlane_b32 s9, v1
	v_readlane_b32 s0, v252, 4
	s_lshl_b32 s0, s0, 8
	v_readlane_b32 s2, v252, 2
	v_readlane_b32 s3, v252, 3
	s_add_u32 s6, s2, s0
	s_addc_u32 s7, s3, 0
	s_mul_i32 s10, s8, 14
	s_mul_i32 s11, s9, 14
	v_mov_b32_e32 v4, 0x1000
	v_mov_b32_e32 v5, 1
	global_atomic_add v4, v4, v5, s[6:7] offset:1024 sc0
	v_mov_b32_e32 v1, 0x3400
	s_waitcnt vmcnt(0)
	v_readfirstlane_b32 s0, v4
	s_add_u32 s0, s0, 1
	s_cmp_lg_u32 s0, s10
	s_cbranch_scc1 .Lgbw_13
	buffer_wbl2 sc1
	s_waitcnt vmcnt(0)
	global_atomic_add v1, v5, s[2:3]

; __device__ __forceinline__ unsigned xb_add(unsigned* p, unsigned v) { return __hip_atomic_fetch_add(p, v, __ATOMIC_RELAXED, __HIP_MEMORY_SCOPE_AGENT); }
; __device__ __forceinline__ void xcd_barrier(const XcdBarrier& b) {
;     ...
;     if (threadIdx.x == 0) {
;         unsigned* bar = b.bar;
;         __builtin_amdgcn_s_waitcnt(0);
;         unsigned nloc = b.st[0], nx = b.st[1];
;         if (nloc == 0u) { xcd_barrier_complete(bar, b.x, nloc, nx); b.st[0] = nloc; b.st[1] = nx; }
;         const unsigned old = xb_add(&bar[XB_XSUB(b.x)], 1u);
;         const unsigned gen = old / nloc;
;         if (old + 1u == (gen + 1u) * nloc) {
;             __builtin_amdgcn_fence(__ATOMIC_RELEASE, "agent");
;             asm volatile("s_waitcnt vmcnt(0)" ::: "memory");
;             const unsigned og = xb_add(&bar[XB_TOP], 1u);
;             const unsigned tg = og / nx;
;             if (og + 1u == (tg + 1u) * nx) xb_add(&bar[XB_TOPGEN], 1u);
.LBB0_1585:
	s_waitcnt lgkmcnt(0)
	v_readfirstlane_b32 s8, v3
	v_readfirstlane_b32 s9, v1
	v_readlane_b32 s0, v252, 4
	s_lshl_b32 s0, s0, 8
	v_readlane_b32 s2, v252, 2
	v_readlane_b32 s3, v252, 3
	s_add_u32 s6, s2, s0
	s_addc_u32 s7, s3, 0
	s_mul_i32 s10, s8, 15
	s_mul_i32 s11, s9, 15
	v_mov_b32_e32 v4, 0x1000
	v_mov_b32_e32 v5, 1
	global_atomic_add v4, v4, v5, s[6:7] offset:1024 sc0
	v_mov_b32_e32 v1, 0x3400
	s_waitcnt vmcnt(0)
	v_readfirstlane_b32 s0, v4
	s_add_u32 s0, s0, 1
	s_cmp_lg_u32 s0, s10
	s_cbranch_scc1 .Lgbw_14
	buffer_wbl2 sc1
	s_waitcnt vmcnt(0)
	global_atomic_add v1, v5, s[2:3]

; __device__ __forceinline__ unsigned xb_add(unsigned* p, unsigned v) { return __hip_atomic_fetch_add(p, v, __ATOMIC_RELAXED, __HIP_MEMORY_SCOPE_AGENT); }
; __device__ __forceinline__ void xcd_barrier(const XcdBarrier& b) {
;     ...
;     if (threadIdx.x == 0) {
;         unsigned* bar = b.bar;
;         __builtin_amdgcn_s_waitcnt(0);
;         unsigned nloc = b.st[0], nx = b.st[1];
;         if (nloc == 0u) { xcd_barrier_complete(bar, b.x, nloc, nx); b.st[0] = nloc; b.st[1] = nx; }
;         const unsigned old = xb_add(&bar[XB_XSUB(b.x)], 1u);
;         const unsigned gen = old / nloc;
;         if (old + 1u == (gen + 1u) * nloc) {
;             __builtin_amdgcn_fence(__ATOMIC_RELEASE, "agent");
;             asm volatile("s_waitcnt vmcnt(0)" ::: "memory");
;             const unsigned og = xb_add(&bar[XB_TOP], 1u);
;             const unsigned tg = og / nx;
;             if (og + 1u == (tg + 1u) * nx) xb_add(&bar[XB_TOPGEN], 1u);
.LBB0_1653:
	s_waitcnt lgkmcnt(0)
	v_readfirstlane_b32 s8, v3
	v_readfirstlane_b32 s9, v1
	v_readlane_b32 s0, v252, 4
	s_lshl_b32 s0, s0, 8
	v_readlane_b32 s2, v252, 2
	v_readlane_b32 s3, v252, 3
	s_add_u32 s6, s2, s0
	s_addc_u32 s7, s3, 0
	s_mul_i32 s10, s8, 16
	s_mul_i32 s11, s9, 16
	v_mov_b32_e32 v4, 0x1000
	v_mov_b32_e32 v5, 1
	global_atomic_add v4, v4, v5, s[6:7] offset:1024 sc0
	v_mov_b32_e32 v1, 0x3400
	s_waitcnt vmcnt(0)
	v_readfirstlane_b32 s0, v4
	s_add_u32 s0, s0, 1
	s_cmp_lg_u32 s0, s10
	s_cbranch_scc1 .Lgbw_15
	buffer_wbl2 sc1
	s_waitcnt vmcnt(0)
	global_atomic_add v1, v5, s[2:3]

; __device__ __forceinline__ unsigned xb_add(unsigned* p, unsigned v) { return __hip_atomic_fetch_add(p, v, __ATOMIC_RELAXED, __HIP_MEMORY_SCOPE_AGENT); }
; __device__ __forceinline__ void xcd_barrier(const XcdBarrier& b) {
;     ...
;     if (threadIdx.x == 0) {
;         unsigned* bar = b.bar;
;         __builtin_amdgcn_s_waitcnt(0);
;         unsigned nloc = b.st[0], nx = b.st[1];
;         if (nloc == 0u) { xcd_barrier_complete(bar, b.x, nloc, nx); b.st[0] = nloc; b.st[1] = nx; }
;         const unsigned old = xb_add(&bar[XB_XSUB(b.x)], 1u);
;         const unsigned gen = old / nloc;
;         if (old + 1u == (gen + 1u) * nloc) {
;             __builtin_amdgcn_fence(__ATOMIC_RELEASE, "agent");
;             asm volatile("s_waitcnt vmcnt(0)" ::: "memory");
;             const unsigned og = xb_add(&bar[XB_TOP], 1u);
;             const unsigned tg = og / nx;
;             if (og + 1u == (tg + 1u) * nx) xb_add(&bar[XB_TOPGEN], 1u);
.LBB0_1721:
	s_waitcnt lgkmcnt(0)
	v_readfirstlane_b32 s8, v3
	v_readfirstlane_b32 s9, v1
	v_readlane_b32 s0, v252, 4
	s_lshl_b32 s0, s0, 8
	v_readlane_b32 s2, v252, 2
	v_readlane_b32 s3, v252, 3
	s_add_u32 s6, s2, s0
	s_addc_u32 s7, s3, 0
	s_mul_i32 s10, s8, 17
	s_mul_i32 s11, s9, 17
	v_mov_b32_e32 v4, 0x1000
	v_mov_b32_e32 v5, 1
	global_atomic_add v4, v4, v5, s[6:7] offset:1024 sc0
	v_mov_b32_e32 v1, 0x3400
	s_waitcnt vmcnt(0)
	v_readfirstlane_b32 s0, v4
	s_add_u32 s0, s0, 1
	s_cmp_lg_u32 s0, s10
	s_cbranch_scc1 .Lgbw_16
	buffer_wbl2 sc1
	s_waitcnt vmcnt(0)
	global_atomic_add v1, v5, s[2:3]

; __device__ __forceinline__ unsigned xb_add(unsigned* p, unsigned v) { return __hip_atomic_fetch_add(p, v, __ATOMIC_RELAXED, __HIP_MEMORY_SCOPE_AGENT); }
; __device__ __forceinline__ void xcd_barrier(const XcdBarrier& b) {
;     ...
;     if (threadIdx.x == 0) {
;         unsigned* bar = b.bar;
;         __builtin_amdgcn_s_waitcnt(0);
;         unsigned nloc = b.st[0], nx = b.st[1];
;         if (nloc == 0u) { xcd_barrier_complete(bar, b.x, nloc, nx); b.st[0] = nloc; b.st[1] = nx; }
;         const unsigned old = xb_add(&bar[XB_XSUB(b.x)], 1u);
;         const unsigned gen = old / nloc;
;         if (old + 1u == (gen + 1u) * nloc) {
;             __builtin_amdgcn_fence(__ATOMIC_RELEASE, "agent");
;             asm volatile("s_waitcnt vmcnt(0)" ::: "memory");
;             const unsigned og = xb_add(&bar[XB_TOP], 1u);
;             const unsigned tg = og / nx;
;             if (og + 1u == (tg + 1u) * nx) xb_add(&bar[XB_TOPGEN], 1u);
.LBB0_1855:
	s_waitcnt lgkmcnt(0)
	v_readfirstlane_b32 s8, v3
	v_readfirstlane_b32 s9, v1
	v_readlane_b32 s0, v252, 4
	s_lshl_b32 s0, s0, 8
	v_readlane_b32 s2, v252, 2
	v_readlane_b32 s3, v252, 3
	s_add_u32 s6, s2, s0
	s_addc_u32 s7, s3, 0
	s_mul_i32 s10, s8, 18
	s_mul_i32 s11, s9, 18
	v_mov_b32_e32 v4, 0x1000
	v_mov_b32_e32 v5, 1
	global_atomic_add v4, v4, v5, s[6:7] offset:1024 sc0
	v_mov_b32_e32 v1, 0x3400
	s_waitcnt vmcnt(0)
	v_readfirstlane_b32 s0, v4
	s_add_u32 s0, s0, 1
	s_cmp_lg_u32 s0, s10
	s_cbranch_scc1 .Lgbw_17
	buffer_wbl2 sc1
	s_waitcnt vmcnt(0)
	global_atomic_add v1, v5, s[2:3]

; __device__ __forceinline__ unsigned xb_add(unsigned* p, unsigned v) { return __hip_atomic_fetch_add(p, v, __ATOMIC_RELAXED, __HIP_MEMORY_SCOPE_AGENT); }
; __device__ __forceinline__ void xcd_barrier(const XcdBarrier& b) {
;     ...
;     if (threadIdx.x == 0) {
;         unsigned* bar = b.bar;
;         __builtin_amdgcn_s_waitcnt(0);
;         unsigned nloc = b.st[0], nx = b.st[1];
;         if (nloc == 0u) { xcd_barrier_complete(bar, b.x, nloc, nx); b.st[0] = nloc; b.st[1] = nx; }
;         const unsigned old = xb_add(&bar[XB_XSUB(b.x)], 1u);
;         const unsigned gen = old / nloc;
;         if (old + 1u == (gen + 1u) * nloc) {
;             __builtin_amdgcn_fence(__ATOMIC_RELEASE, "agent");
;             asm volatile("s_waitcnt vmcnt(0)" ::: "memory");
;             const unsigned og = xb_add(&bar[XB_TOP], 1u);
;             const unsigned tg = og / nx;
;             if (og + 1u == (tg + 1u) * nx) xb_add(&bar[XB_TOPGEN], 1u);
.LBB0_1999:
	s_waitcnt lgkmcnt(0)
	v_readfirstlane_b32 s8, v3
	v_readfirstlane_b32 s9, v1
	v_readlane_b32 s0, v252, 4
	s_lshl_b32 s0, s0, 8
	v_readlane_b32 s2, v252, 2
	v_readlane_b32 s3, v252, 3
	s_add_u32 s6, s2, s0
	s_addc_u32 s7, s3, 0
	s_mul_i32 s10, s8, 19
	s_mul_i32 s11, s9, 19
	v_mov_b32_e32 v4, 0x1000
	v_mov_b32_e32 v5, 1
	global_atomic_add v4, v4, v5, s[6:7] offset:1024 sc0
	v_mov_b32_e32 v1, 0x3400
	s_waitcnt vmcnt(0)
	v_readfirstlane_b32 s0, v4
	s_add_u32 s0, s0, 1
	s_cmp_lg_u32 s0, s10
	s_cbranch_scc1 .Lgbw_18
	buffer_wbl2 sc1
	s_waitcnt vmcnt(0)
	global_atomic_add v1, v5, s[2:3]
